# adds: pconv all 16 loads of the four trips issued first (256-workgroup grid fast path)
# baseline (speedup 1.0000x reference)
; __device__ __forceinline__ u32x4 pack8(f32x4 a, f32x4 b) { u32x4 w; w.x = pk2(a[0], a[1]); w.y = pk2(a[2], a[3]); w.z = pk2(b[0], b[1]); w.w = pk2(b[2], b[3]); return w; }
; template <class Tp> __device__ __forceinline__ Tp* wsp(const Frame& F, size_t off) { return (Tp*)(F.ws + off); }
; __device__ __forceinline__ void phase_pconv(Frame& F, int l) {
;     const Params& P = *F.P; bf16_t* PB = wsp<bf16_t>(F, WS_PB); const float* pl = P.in[1] + (size_t)l * T * DPLE;
;     for (int i = F.bx * NTHREADS + F.tid; i < T * DPLE / 16; i += F.G * NTHREADS) {
;         const f32x4* pp = (const f32x4*)(pl + (size_t)i * 16); const f32x4 a = pp[0], b2 = pp[1], c2 = pp[2], d2 = pp[3];
;         u32x4* dst = (u32x4*)(PB + (size_t)i * 16); dst[0] = pack8(a, b2); dst[1] = pack8(c2, d2); }
; }
.LBB0_1469:
	s_or_b64 exec, exec, s[44:45]
	s_cmp_eq_u32 s62, 3
	s_waitcnt lgkmcnt(0)
	s_barrier
	s_cbranch_scc1 .LBB0_1474
	v_readlane_b32 s2, v253, 3
	s_nop 1
	v_add_u32_e32 v2, s2, v188
	s_mov_b32 s2, 0x80000
	v_cmp_gt_i32_e32 vcc, s2, v2
	s_and_saveexec_b64 s[10:11], vcc
	v_readlane_b32 s16, v255, 28
	v_readlane_b32 s18, v255, 30
	v_readlane_b32 s6, v255, 26
	v_readlane_b32 s17, v255, 29
	v_readlane_b32 s19, v255, 31
	v_readlane_b32 s7, v255, 27
	s_cbranch_execz .LBB0_1473
	v_ashrrev_i32_e32 v3, 31, v2
	v_lshlrev_b64 v[6:7], 5, v[2:3]
	v_lshl_add_u64 v[6:7], s[74:75], 0, v[6:7]
	s_mov_b64 s[2:3], 0x2ac00010
	v_readlane_b32 s14, v254, 51
	v_lshlrev_b64 v[4:5], 6, v[2:3]
	v_lshl_add_u64 v[6:7], v[6:7], 0, s[2:3]
	s_mov_b64 s[12:13], 0
	v_readlane_b32 s15, v254, 52
	s_cmp_lg_u32 s6, 0x20000
	s_cbranch_scc1 .LBB0_1472
	v_lshl_add_u64 v[20:21], s[14:15], 0, v[4:5]
	global_load_dwordx4 v[24:27], v[20:21], off
	global_load_dwordx4 v[28:31], v[20:21], off offset:16
	global_load_dwordx4 v[32:35], v[20:21], off offset:32
	global_load_dwordx4 v[36:39], v[20:21], off offset:48
	s_add_u32 s14, s14, s16
	s_addc_u32 s15, s15, s17
	v_lshl_add_u64 v[20:21], s[14:15], 0, v[4:5]
	global_load_dwordx4 v[40:43], v[20:21], off
	global_load_dwordx4 v[44:47], v[20:21], off offset:16
	global_load_dwordx4 v[48:51], v[20:21], off offset:32
	global_load_dwordx4 v[52:55], v[20:21], off offset:48
	s_add_u32 s14, s14, s16
	s_addc_u32 s15, s15, s17
	v_lshl_add_u64 v[20:21], s[14:15], 0, v[4:5]
	global_load_dwordx4 v[56:59], v[20:21], off
	global_load_dwordx4 v[60:63], v[20:21], off offset:16
	global_load_dwordx4 v[64:67], v[20:21], off offset:32
	global_load_dwordx4 v[68:71], v[20:21], off offset:48
	s_add_u32 s14, s14, s16
	s_addc_u32 s15, s15, s17
	v_lshl_add_u64 v[20:21], s[14:15], 0, v[4:5]
	global_load_dwordx4 v[72:75], v[20:21], off
	global_load_dwordx4 v[76:79], v[20:21], off offset:16
	global_load_dwordx4 v[80:83], v[20:21], off offset:32
	global_load_dwordx4 v[84:87], v[20:21], off offset:48
	s_add_u32 s14, s14, s16
	s_addc_u32 s15, s15, s17
	s_waitcnt vmcnt(12)
	v_cvt_pk_bf16_f32 v8, v24, v25
	v_cvt_pk_bf16_f32 v9, v26, v27
	v_cvt_pk_bf16_f32 v10, v28, v29
	v_cvt_pk_bf16_f32 v11, v30, v31
	v_cvt_pk_bf16_f32 v12, v32, v33
	v_cvt_pk_bf16_f32 v13, v34, v35
	v_cvt_pk_bf16_f32 v14, v36, v37
	v_cvt_pk_bf16_f32 v15, v38, v39
	global_store_dwordx4 v[6:7], v[8:11], off offset:-16
	global_store_dwordx4 v[6:7], v[12:15], off
	s_nop 1
	v_lshl_add_u64 v[6:7], v[6:7], 0, s[18:19]
	s_waitcnt vmcnt(10)
	v_cvt_pk_bf16_f32 v8, v40, v41
	v_cvt_pk_bf16_f32 v9, v42, v43
	v_cvt_pk_bf16_f32 v10, v44, v45
	v_cvt_pk_bf16_f32 v11, v46, v47
	v_cvt_pk_bf16_f32 v12, v48, v49
	v_cvt_pk_bf16_f32 v13, v50, v51
	v_cvt_pk_bf16_f32 v14, v52, v53
	v_cvt_pk_bf16_f32 v15, v54, v55
	global_store_dwordx4 v[6:7], v[8:11], off offset:-16
	global_store_dwordx4 v[6:7], v[12:15], off
	s_nop 1
	v_lshl_add_u64 v[6:7], v[6:7], 0, s[18:19]
	s_waitcnt vmcnt(8)
	v_cvt_pk_bf16_f32 v8, v56, v57
	v_cvt_pk_bf16_f32 v9, v58, v59
	v_cvt_pk_bf16_f32 v10, v60, v61
	v_cvt_pk_bf16_f32 v11, v62, v63
	v_cvt_pk_bf16_f32 v12, v64, v65
	v_cvt_pk_bf16_f32 v13, v66, v67
	v_cvt_pk_bf16_f32 v14, v68, v69
	v_cvt_pk_bf16_f32 v15, v70, v71
	global_store_dwordx4 v[6:7], v[8:11], off offset:-16
	global_store_dwordx4 v[6:7], v[12:15], off
	s_nop 1
	v_lshl_add_u64 v[6:7], v[6:7], 0, s[18:19]
	s_waitcnt vmcnt(6)
	v_cvt_pk_bf16_f32 v8, v72, v73
	v_cvt_pk_bf16_f32 v9, v74, v75
	v_cvt_pk_bf16_f32 v10, v76, v77
	v_cvt_pk_bf16_f32 v11, v78, v79
	v_cvt_pk_bf16_f32 v12, v80, v81
	v_cvt_pk_bf16_f32 v13, v82, v83
	v_cvt_pk_bf16_f32 v14, v84, v85
	v_cvt_pk_bf16_f32 v15, v86, v87
	global_store_dwordx4 v[6:7], v[8:11], off offset:-16
	global_store_dwordx4 v[6:7], v[12:15], off
	s_nop 1
	v_lshl_add_u64 v[6:7], v[6:7], 0, s[18:19]
	s_branch .LBB0_1473
